# attention phase: one static s_setprio 1 for the younger wave half (waves 4-7), back to 0 at the next phase
# speedup vs baseline: 1.0033x; 1.0033x over previous
.LBB0_2639:
	s_cmp_lt_i32 s56, 12
	s_cselect_b64 s[0:1], -1, 0
	s_cmp_gt_i32 s57, 11
	s_cselect_b64 s[2:3], -1, 0
	s_and_b64 s[0:1], s[0:1], s[2:3]
	s_andn2_b64 vcc, exec, s[0:1]
	s_cbranch_vccnz .LBB0_3508
	v_readfirstlane_b32 s98, v0
	s_nop 3
	s_bitcmp1_b32 s98, 8
	s_cbranch_scc0 .Lattn_old
	s_setprio 1
